# hyena latent unit: shifted filter copies built from 8-byte LDS reads + v_alignbit instead of 12 iterations of conditional ds_read_u16 per thread (both layers)
# baseline (speedup 1.0000x reference)
; #define LAS __attribute__((address_space(3)))
;     ...
;         { const bf16* fsrc = (L == SL) ? WSP(bf16, WS_FILT) + (size_t)((l * 2 + o) * 512 + c) * (2 * L) : WSP(bf16, WS_FILTC) + (size_t)(o * 512 + c) * (2 * L);
;           constexpr int N2 = (L / 4) / NT; u32x4 t2[N2];
; #pragma unroll
;           for (int i = 0; i < N2; ++i) t2[i] = *(const u32x4*)(fsrc + 8 * (C.tid + NT * i));
; #pragma unroll
;           for (int i = 0; i < N2; ++i) *(LAS u32x4*)(C.lds + R_OFF + 16 * (C.tid + NT * i)) = t2[i]; }
;         __syncthreads();
;         for (int idx = C.tid; idx < 3 * (L / 2); idx += NT) { const int p = 1 + idx / (L / 2), w = idx % (L / 2); unsigned short e[4];
; #pragma unroll
;             for (int k = 0; k < 4; ++k) { const int n = 4 * w + p + k; e[k] = n < 2 * L ? *(const LAS bf16*)(C.lds + R_OFF + 2 * n) : (bf16)0; }
;             *(LAS u32x2*)(C.lds + R_OFF + p * CSZ + 8 + 64 * p + 8 * w) = (u32x2){(unsigned)e[0] | ((unsigned)e[1] << 16), (unsigned)e[2] | ((unsigned)e[3] << 16)}; }
.LBB0_917:
	s_add_i32 s10, s12, s42
	s_ashr_i32 s11, s10, 31
	s_lshl_b64 s[12:13], s[10:11], 14
	s_add_u32 s12, s19, s12
	s_addc_u32 s13, s24, s13
	v_lshl_add_u64 v[2:3], v[164:165], 1, s[12:13]
	v_lshl_add_u64 v[6:7], v[166:167], 1, s[12:13]
	global_load_dwordx4 v[2:5], v[2:3], off
	s_nop 0
	global_load_dwordx4 v[6:9], v[6:7], off
	v_add_u32_e32 v10, 0, v213
	s_waitcnt vmcnt(1)
	ds_write_b128 v10, v[2:5] offset:32896
	s_waitcnt vmcnt(0)
	ds_write_b128 v10, v[6:9] offset:41088
	s_waitcnt lgkmcnt(0)
	s_barrier
	s_and_saveexec_b64 s[12:13], s[6:7]
	s_cbranch_execz .LBB0_926
	v_lshlrev_b32_e32 v2, 3, v212
	v_add_u32_e32 v3, 0x8000, v2
	ds_read_b64 v[4:5], v2 offset:32896
	ds_read_b64 v[6:7], v2 offset:32904
	ds_read_b64 v[8:9], v2 offset:36992
	ds_read_b64 v[10:11], v2 offset:37000
	ds_read_b64 v[12:13], v2 offset:41088
	ds_read_b64 v[14:15], v2 offset:41096
	ds_read_b64 v[16:17], v2 offset:45184
	ds_read_b64 v[18:19], v2 offset:45192
	v_cmp_ne_u32_e32 vcc, 0x1ff, v212
	s_waitcnt lgkmcnt(0)
	v_cndmask_b32_e32 v18, 0, v18, vcc
	v_cndmask_b32_e32 v19, 0, v19, vcc
	v_alignbit_b32 v20, v5, v4, 16
	v_alignbit_b32 v21, v6, v5, 16
	v_mov_b32_e32 v22, v5
	v_mov_b32_e32 v23, v6
	v_mov_b32_e32 v24, v21
	v_alignbit_b32 v25, v7, v6, 16
	ds_write_b64 v2, v[20:21] offset:49352
	ds_write_b64 v3, v[22:23] offset:33032
	ds_write_b64 v3, v[24:25] offset:49480
	s_nop 0
	v_alignbit_b32 v20, v9, v8, 16
	v_alignbit_b32 v21, v10, v9, 16
	v_mov_b32_e32 v22, v9
	v_mov_b32_e32 v23, v10
	v_mov_b32_e32 v24, v21
	v_alignbit_b32 v25, v11, v10, 16
	ds_write_b64 v2, v[20:21] offset:53448
	ds_write_b64 v3, v[22:23] offset:37128
	ds_write_b64 v3, v[24:25] offset:53576
	s_nop 0
	v_alignbit_b32 v20, v13, v12, 16
	v_alignbit_b32 v21, v14, v13, 16
	v_mov_b32_e32 v22, v13
	v_mov_b32_e32 v23, v14
	v_mov_b32_e32 v24, v21
	v_alignbit_b32 v25, v15, v14, 16
	ds_write_b64 v2, v[20:21] offset:57544
	ds_write_b64 v3, v[22:23] offset:41224
	ds_write_b64 v3, v[24:25] offset:57672
	s_nop 0
	v_alignbit_b32 v20, v17, v16, 16
	v_alignbit_b32 v21, v18, v17, 16
	v_mov_b32_e32 v22, v17
	v_mov_b32_e32 v23, v18
	v_mov_b32_e32 v24, v21
	v_alignbit_b32 v25, v19, v18, 16
	ds_write_b64 v2, v[20:21] offset:61640
	ds_write_b64 v3, v[22:23] offset:45320
	ds_write_b64 v3, v[24:25] offset:61768
	s_nop 0

; #define LAS __attribute__((address_space(3)))
;     ...
;         { const bf16* fsrc = (L == SL) ? WSP(bf16, WS_FILT) + (size_t)((l * 2 + o) * 512 + c) * (2 * L) : WSP(bf16, WS_FILTC) + (size_t)(o * 512 + c) * (2 * L);
;           constexpr int N2 = (L / 4) / NT; u32x4 t2[N2];
; #pragma unroll
;           for (int i = 0; i < N2; ++i) t2[i] = *(const u32x4*)(fsrc + 8 * (C.tid + NT * i));
; #pragma unroll
;           for (int i = 0; i < N2; ++i) *(LAS u32x4*)(C.lds + R_OFF + 16 * (C.tid + NT * i)) = t2[i]; }
;         __syncthreads();
;         for (int idx = C.tid; idx < 3 * (L / 2); idx += NT) { const int p = 1 + idx / (L / 2), w = idx % (L / 2); unsigned short e[4];
; #pragma unroll
;             for (int k = 0; k < 4; ++k) { const int n = 4 * w + p + k; e[k] = n < 2 * L ? *(const LAS bf16*)(C.lds + R_OFF + 2 * n) : (bf16)0; }
;             *(LAS u32x2*)(C.lds + R_OFF + p * CSZ + 8 + 64 * p + 8 * w) = (u32x2){(unsigned)e[0] | ((unsigned)e[1] << 16), (unsigned)e[2] | ((unsigned)e[3] << 16)}; }
.LBB0_2072:
	s_add_i32 s10, s35, s46
	s_ashr_i32 s11, s10, 31
	s_lshl_b64 s[12:13], s[10:11], 14
	s_add_u32 s12, s18, s12
	s_addc_u32 s13, s19, s13
	v_lshl_add_u64 v[2:3], v[164:165], 1, s[12:13]
	v_lshl_add_u64 v[6:7], v[166:167], 1, s[12:13]
	global_load_dwordx4 v[2:5], v[2:3], off
	s_nop 0
	global_load_dwordx4 v[6:9], v[6:7], off
	v_add_u32_e32 v10, 0, v213
	s_waitcnt vmcnt(1)
	ds_write_b128 v10, v[2:5] offset:32896
	s_waitcnt vmcnt(0)
	ds_write_b128 v10, v[6:9] offset:41088
	s_waitcnt lgkmcnt(0)
	s_barrier
	s_and_saveexec_b64 s[12:13], s[6:7]
	s_cbranch_execz .LBB0_2081
	v_lshlrev_b32_e32 v2, 3, v212
	v_add_u32_e32 v3, 0x8000, v2
	ds_read_b64 v[4:5], v2 offset:32896
	ds_read_b64 v[6:7], v2 offset:32904
	ds_read_b64 v[8:9], v2 offset:36992
	ds_read_b64 v[10:11], v2 offset:37000
	ds_read_b64 v[12:13], v2 offset:41088
	ds_read_b64 v[14:15], v2 offset:41096
	ds_read_b64 v[16:17], v2 offset:45184
	ds_read_b64 v[18:19], v2 offset:45192
	v_cmp_ne_u32_e32 vcc, 0x1ff, v212
	s_waitcnt lgkmcnt(0)
	v_cndmask_b32_e32 v18, 0, v18, vcc
	v_cndmask_b32_e32 v19, 0, v19, vcc
	v_alignbit_b32 v20, v5, v4, 16
	v_alignbit_b32 v21, v6, v5, 16
	v_mov_b32_e32 v22, v5
	v_mov_b32_e32 v23, v6
	v_mov_b32_e32 v24, v21
	v_alignbit_b32 v25, v7, v6, 16
	ds_write_b64 v2, v[20:21] offset:49352
	ds_write_b64 v3, v[22:23] offset:33032
	ds_write_b64 v3, v[24:25] offset:49480
	s_nop 0
	v_alignbit_b32 v20, v9, v8, 16
	v_alignbit_b32 v21, v10, v9, 16
	v_mov_b32_e32 v22, v9
	v_mov_b32_e32 v23, v10
	v_mov_b32_e32 v24, v21
	v_alignbit_b32 v25, v11, v10, 16
	ds_write_b64 v2, v[20:21] offset:53448
	ds_write_b64 v3, v[22:23] offset:37128
	ds_write_b64 v3, v[24:25] offset:53576
	s_nop 0
	v_alignbit_b32 v20, v13, v12, 16
	v_alignbit_b32 v21, v14, v13, 16
	v_mov_b32_e32 v22, v13
	v_mov_b32_e32 v23, v14
	v_mov_b32_e32 v24, v21
	v_alignbit_b32 v25, v15, v14, 16
	ds_write_b64 v2, v[20:21] offset:57544
	ds_write_b64 v3, v[22:23] offset:41224
	ds_write_b64 v3, v[24:25] offset:57672
	s_nop 0
	v_alignbit_b32 v20, v17, v16, 16
	v_alignbit_b32 v21, v18, v17, 16
	v_mov_b32_e32 v22, v17
	v_mov_b32_e32 v23, v18
	v_mov_b32_e32 v24, v21
	v_alignbit_b32 v25, v19, v18, 16
	ds_write_b64 v2, v[20:21] offset:61640
	ds_write_b64 v3, v[22:23] offset:45320
	ds_write_b64 v3, v[24:25] offset:61768
	s_nop 0
